# s22 + P3 on 224 workgroups with 32 converter workgroups taking 6144 gate_up items of P4's slice (P3 leaves HBM bandwidth unused, P4 is bound by it); seam second items on workgroups 192..
# speedup vs baseline: 1.0055x; 1.0055x over previous
; #define LAS __attribute__((address_space(3)))
; __global__ void __launch_bounds__(NTHREADS, 2) fwd(Args args) {
;     ...
;     if (IN(3)) {
;         LAS float* LRs = (LAS float*)lds;
;         LAS float* PART = (LAS float*)(lds + 8192);
;         LAS bf16* QEs = (LAS bf16*)(lds + 10240);
;         LAS bf16* KEs = (LAS bf16*)(lds + 27648);
;         LAS bf16* ATTs = (LAS bf16*)(lds + 45056);
;         LAS bf16* VTs = (LAS bf16*)(lds + 54272);
;         LAS bf16* Qs = (LAS bf16*)(lds + 91136);
;         LAS bf16* Ks = (LAS bf16*)(lds + 108544);
;         float wg[2][16], bias2[2]; int hprev = -1;
;         for (int u = bid; u < NBATCH * 68 * 4; u += G) {
.LBB0_350:
	s_cmp_lt_i32 s90, 4
	s_cselect_b64 s[2:3], -1, 0
	s_add_u32 s68, s88, 0x6a800000
	s_addc_u32 s69, s89, 0
	s_and_b64 s[4:5], s[2:3], s[0:1]
	s_xor_b64 s[0:1], s[4:5], -1
	s_cmpk_gt_i32 s94, 0x43f
	s_cselect_b64 s[2:3], -1, 0
	s_or_b64 s[0:1], s[0:1], s[2:3]
	s_and_b64 vcc, exec, s[0:1]
	v_lshl_add_u32 v1, v0, 2, 0
	s_cbranch_vccnz .LBB0_370
	v_readlane_b32 s16, v246, 23
	s_nop 3
	s_cmp_ge_u32 s94, s16
	s_cbranch_scc0 .Lfc3_skip
	v_writelane_b32 v247, s4, 0
	v_writelane_b32 v247, s5, 1
	v_readlane_b32 s3, v246, 21
	v_readlane_b32 s2, v246, 23
	s_nop 3
	s_sub_i32 s2, s94, s2
	s_lshl_b32 s2, s2, 3
	s_add_i32 s2, s2, s3
	s_mov_b32 s4, 6144
	s_cmp_lt_u32 s2, s4
	s_cbranch_scc0 .Lfc3_done
	v_mbcnt_lo_u32_b32 v208, -1, 0
	v_mbcnt_hi_u32_b32 v208, -1, v208
	v_lshrrev_b32_e32 v204, 3, v208
	v_and_b32_e32 v208, 7, v208
	v_lshlrev_b32_e32 v205, 4, v208
	v_lshlrev_b32_e32 v206, 13, v208
	v_lshl_add_u32 v206, v204, 4, v206
	v_readlane_b32 s14, v246, 8
	v_readlane_b32 s15, v246, 9
	s_nop 3
	s_sub_u32 s14, s14, 0x100
	s_subb_u32 s15, s15, 0
	s_load_dwordx2 s[18:19], s[14:15], 0xb8
	s_load_dwordx2 s[20:21], s[14:15], 0xc8
	s_mov_b32 s22, 0x43800000
	s_mov_b32 s23, 0x43800000
	s_mov_b32 s5, 0
	s_mov_b32 s3, s2
	s_waitcnt vmcnt(0) lgkmcnt(0)
	s_mov_b32 s26, 53760
	s_add_u32 s29, s2, s26
	s_cmp_lt_u32 s29, 0x10000
	s_cbranch_scc0 .Lfc3_sdp0
	s_lshr_b32 s30, s29, 11
	s_and_b32 s26, s29, 0x7ff
	s_lshr_b32 s31, s26, 7
	s_and_b32 s32, s26, 0x7f
	s_lshl_b32 s26, s30, 25
	s_lshl_b32 s27, s31, 21
	s_add_u32 s26, s26, s27
	s_lshl_b32 s27, s32, 7
	s_add_u32 s26, s26, s27
	s_add_u32 s6, s18, s26
	s_addc_u32 s7, s19, 0
	s_movk_i32 s24, 0x4000
	s_branch .Lfc3_scp0

; __device__ __forceinline__ void item8_load(const float* W, int N, int k0, int n0, int lane, f32x4 (&rg)[16]) {
; #pragma unroll
;     for (int i = 0; i < 16; ++i) rg[i] = __builtin_nontemporal_load((const f32x4*)(W + (size_t)(k0 + 8 * i + (lane >> 3)) * N + n0 + 4 * (lane & 7)));
; }
.Lfc3_scp0:
	s_lshl_b32 s25, s24, 4
	v_mad_u32_u24 v207, v204, s25, v205
	global_load_dwordx4 v[2:5], v207, s[6:7] nt
	s_add_u32 s6, s6, s24
	s_addc_u32 s7, s7, 0
	global_load_dwordx4 v[6:9], v207, s[6:7] nt
	s_add_u32 s6, s6, s24
	s_addc_u32 s7, s7, 0
	global_load_dwordx4 v[10:13], v207, s[6:7] nt
	s_add_u32 s6, s6, s24
	s_addc_u32 s7, s7, 0
	global_load_dwordx4 v[14:17], v207, s[6:7] nt
	s_add_u32 s6, s6, s24
	s_addc_u32 s7, s7, 0
	global_load_dwordx4 v[18:21], v207, s[6:7] nt
	s_add_u32 s6, s6, s24
	s_addc_u32 s7, s7, 0
	global_load_dwordx4 v[22:25], v207, s[6:7] nt
	s_add_u32 s6, s6, s24
	s_addc_u32 s7, s7, 0
	global_load_dwordx4 v[26:29], v207, s[6:7] nt
	s_add_u32 s6, s6, s24
	s_addc_u32 s7, s7, 0
	global_load_dwordx4 v[30:33], v207, s[6:7] nt
	s_add_u32 s6, s6, s24
	s_addc_u32 s7, s7, 0
	global_load_dwordx4 v[34:37], v207, s[6:7] nt
	s_add_u32 s6, s6, s24
	s_addc_u32 s7, s7, 0
	global_load_dwordx4 v[38:41], v207, s[6:7] nt
	s_add_u32 s6, s6, s24
	s_addc_u32 s7, s7, 0
	global_load_dwordx4 v[42:45], v207, s[6:7] nt
	s_add_u32 s6, s6, s24
	s_addc_u32 s7, s7, 0
	global_load_dwordx4 v[46:49], v207, s[6:7] nt
	s_add_u32 s6, s6, s24
	s_addc_u32 s7, s7, 0
	global_load_dwordx4 v[50:53], v207, s[6:7] nt
	s_add_u32 s6, s6, s24
	s_addc_u32 s7, s7, 0
	global_load_dwordx4 v[54:57], v207, s[6:7] nt
	s_add_u32 s6, s6, s24
	s_addc_u32 s7, s7, 0
	global_load_dwordx4 v[58:61], v207, s[6:7] nt
	s_add_u32 s6, s6, s24
	s_addc_u32 s7, s7, 0
	global_load_dwordx4 v[62:65], v207, s[6:7] nt
	s_add_u32 s2, s2, 256
	s_cmp_lt_u32 s2, s4
	s_cbranch_scc0 .Lfc3_body0
	s_mov_b32 s26, 53760
	s_add_u32 s29, s2, s26
	s_cmp_lt_u32 s29, 0x10000
	s_cbranch_scc0 .Lfc3_sdp1
	s_lshr_b32 s30, s29, 11
	s_and_b32 s26, s29, 0x7ff
	s_lshr_b32 s31, s26, 7
	s_and_b32 s32, s26, 0x7f
	s_lshl_b32 s26, s30, 25
	s_lshl_b32 s27, s31, 21
	s_add_u32 s26, s26, s27
	s_lshl_b32 s27, s32, 7
	s_add_u32 s26, s26, s27
	s_add_u32 s6, s18, s26
	s_addc_u32 s7, s19, 0
	s_movk_i32 s24, 0x4000
	s_branch .Lfc3_scp1

.Lfc3_body0:
	s_add_u32 s2, s2, 256
	s_cmp_lt_u32 s2, s4
	s_cbranch_scc0 .Lfc3_nl0
	s_mov_b32 s26, 53760
	s_add_u32 s29, s2, s26
	s_cmp_lt_u32 s29, 0x10000
	s_cbranch_scc0 .Lfc3_sdb0
	s_lshr_b32 s30, s29, 11
	s_and_b32 s26, s29, 0x7ff
	s_lshr_b32 s31, s26, 7
	s_and_b32 s32, s26, 0x7f
	s_lshl_b32 s26, s30, 25
	s_lshl_b32 s27, s31, 21
	s_add_u32 s26, s26, s27
	s_lshl_b32 s27, s32, 7
	s_add_u32 s26, s26, s27
	s_add_u32 s6, s18, s26
	s_addc_u32 s7, s19, 0
	s_movk_i32 s24, 0x4000
	s_branch .Lfc3_scb0

; __device__ __forceinline__ void item8_load(const float* W, int N, int k0, int n0, int lane, f32x4 (&rg)[16]) {
; #pragma unroll
;     for (int i = 0; i < 16; ++i) rg[i] = __builtin_nontemporal_load((const f32x4*)(W + (size_t)(k0 + 8 * i + (lane >> 3)) * N + n0 + 4 * (lane & 7)));
; }
.Lfc3_scb0:
	s_lshl_b32 s25, s24, 4
	v_mad_u32_u24 v207, v204, s25, v205
	global_load_dwordx4 v[130:133], v207, s[6:7] nt
	s_add_u32 s6, s6, s24
	s_addc_u32 s7, s7, 0
	global_load_dwordx4 v[134:137], v207, s[6:7] nt
	s_add_u32 s6, s6, s24
	s_addc_u32 s7, s7, 0
	global_load_dwordx4 v[138:141], v207, s[6:7] nt
	s_add_u32 s6, s6, s24
	s_addc_u32 s7, s7, 0
	global_load_dwordx4 v[142:145], v207, s[6:7] nt
	s_add_u32 s6, s6, s24
	s_addc_u32 s7, s7, 0
	global_load_dwordx4 v[146:149], v207, s[6:7] nt
	s_add_u32 s6, s6, s24
	s_addc_u32 s7, s7, 0
	global_load_dwordx4 v[150:153], v207, s[6:7] nt
	s_add_u32 s6, s6, s24
	s_addc_u32 s7, s7, 0
	global_load_dwordx4 v[154:157], v207, s[6:7] nt
	s_add_u32 s6, s6, s24
	s_addc_u32 s7, s7, 0
	global_load_dwordx4 v[158:161], v207, s[6:7] nt
	s_add_u32 s6, s6, s24
	s_addc_u32 s7, s7, 0
	global_load_dwordx4 v[162:165], v207, s[6:7] nt
	s_add_u32 s6, s6, s24
	s_addc_u32 s7, s7, 0
	global_load_dwordx4 v[166:169], v207, s[6:7] nt
	s_add_u32 s6, s6, s24
	s_addc_u32 s7, s7, 0
	global_load_dwordx4 v[170:173], v207, s[6:7] nt
	s_add_u32 s6, s6, s24
	s_addc_u32 s7, s7, 0
	global_load_dwordx4 v[174:177], v207, s[6:7] nt
	s_add_u32 s6, s6, s24
	s_addc_u32 s7, s7, 0
	global_load_dwordx4 v[178:181], v207, s[6:7] nt
	s_add_u32 s6, s6, s24
	s_addc_u32 s7, s7, 0
	global_load_dwordx4 v[182:185], v207, s[6:7] nt
	s_add_u32 s6, s6, s24
	s_addc_u32 s7, s7, 0
	global_load_dwordx4 v[186:189], v207, s[6:7] nt
	s_add_u32 s6, s6, s24
	s_addc_u32 s7, s7, 0
	global_load_dwordx4 v[190:193], v207, s[6:7] nt
	s_mov_b32 s26, 53760
	s_add_u32 s29, s3, s26
	s_cmp_lt_u32 s29, 0x10000
	s_cbranch_scc0 .Lfc3_ddb0
	s_lshr_b32 s30, s29, 11
	s_and_b32 s26, s29, 0x7ff
	s_lshr_b32 s31, s26, 7
	s_and_b32 s32, s26, 0x7f
	s_and_b32 s26, s32, 63
	s_lshr_b32 s26, s26, 2
	s_lshl_b32 s26, s26, 8
	s_lshr_b32 s27, s32, 6
	s_lshl_b32 s27, s27, 7
	s_add_u32 s26, s26, s27
	s_and_b32 s27, s32, 3
	s_lshl_b32 s27, s27, 5
	s_add_u32 s26, s26, s27
	s_lshl_b32 s26, s26, 11
	s_lshl_b32 s27, s30, 23
	s_add_u32 s26, s26, s27
	s_lshl_b32 s27, s31, 7
	s_add_u32 s26, s26, s27
	s_add_u32 s26, s26, 0x4001000
	s_branch .Lfc3_dcb0

.Lfc3_nl0:
	s_mov_b32 s26, 53760
	s_add_u32 s29, s3, s26
	s_cmp_lt_u32 s29, 0x10000
	s_cbranch_scc0 .Lfc3_ddn0
	s_lshr_b32 s30, s29, 11
	s_and_b32 s26, s29, 0x7ff
	s_lshr_b32 s31, s26, 7
	s_and_b32 s32, s26, 0x7f
	s_and_b32 s26, s32, 63
	s_lshr_b32 s26, s26, 2
	s_lshl_b32 s26, s26, 8
	s_lshr_b32 s27, s32, 6
	s_lshl_b32 s27, s27, 7
	s_add_u32 s26, s26, s27
	s_and_b32 s27, s32, 3
	s_lshl_b32 s27, s27, 5
	s_add_u32 s26, s26, s27
	s_lshl_b32 s26, s26, 11
	s_lshl_b32 s27, s30, 23
	s_add_u32 s26, s26, s27
	s_lshl_b32 s27, s31, 7
	s_add_u32 s26, s26, s27
	s_add_u32 s26, s26, 0x4001000
	s_branch .Lfc3_dcn0

; #define LAS __attribute__((address_space(3)))
; #define LDS_WAIT() asm volatile("s_waitcnt lgkmcnt(0)" ::: "memory")
; __device__ __forceinline__ void item8_finish(int K, unsigned char* WT, int k0, int r0, LAS float* scr, int lane, const f32x4 (&rg)[16]) {
; #pragma unroll
;     for (int i = 0; i < 16; ++i) { LAS float* d = scr + (8 * i + (lane >> 3)) * 33 + 4 * (lane & 7); d[0] = rg[i].x; d[1] = rg[i].y; d[2] = rg[i].z; d[3] = rg[i].w; }
;     LDS_WAIT();
;     const int c = lane & 7;
; #pragma unroll
;     for (int j = 0; j < 4; ++j) { const int n = (lane >> 3) + 8 * j; const LAS float* sp = scr + (16 * c) * 33 + n; int w[4];
; #pragma unroll
;         for (int q = 0; q < 4; ++q) { w[q] = __builtin_amdgcn_cvt_pk_fp8_f32(sp[(4 * q) * 33] * 256.f, sp[(4 * q + 1) * 33] * 256.f, 0, false); w[q] = __builtin_amdgcn_cvt_pk_fp8_f32(sp[(4 * q + 2) * 33] * 256.f, sp[(4 * q + 3) * 33] * 256.f, w[q], true); }
;         u32x4 o; o.x = (unsigned)w[0]; o.y = (unsigned)w[1]; o.z = (unsigned)w[2]; o.w = (unsigned)w[3];
;         __builtin_nontemporal_store(o, (u32x4*)(WT + (size_t)(r0 + n) * K + k0 + 16 * c)); }
.Lfc3_cv0:
	v_pk_mul_f32 v[2:3], v[2:3], s[22:23]
	v_pk_mul_f32 v[4:5], v[4:5], s[22:23]
	v_pk_mul_f32 v[6:7], v[6:7], s[22:23]
	v_pk_mul_f32 v[8:9], v[8:9], s[22:23]
	v_pk_mul_f32 v[10:11], v[10:11], s[22:23]
	v_pk_mul_f32 v[12:13], v[12:13], s[22:23]
	v_pk_mul_f32 v[14:15], v[14:15], s[22:23]
	v_pk_mul_f32 v[16:17], v[16:17], s[22:23]
	v_pk_mul_f32 v[18:19], v[18:19], s[22:23]
	v_pk_mul_f32 v[20:21], v[20:21], s[22:23]
	v_pk_mul_f32 v[22:23], v[22:23], s[22:23]
	v_pk_mul_f32 v[24:25], v[24:25], s[22:23]
	v_pk_mul_f32 v[26:27], v[26:27], s[22:23]
	v_pk_mul_f32 v[28:29], v[28:29], s[22:23]
	v_pk_mul_f32 v[30:31], v[30:31], s[22:23]
	v_pk_mul_f32 v[32:33], v[32:33], s[22:23]
	v_pk_mul_f32 v[34:35], v[34:35], s[22:23]
	v_pk_mul_f32 v[36:37], v[36:37], s[22:23]
	v_pk_mul_f32 v[38:39], v[38:39], s[22:23]
	v_pk_mul_f32 v[40:41], v[40:41], s[22:23]
	v_pk_mul_f32 v[42:43], v[42:43], s[22:23]
	v_pk_mul_f32 v[44:45], v[44:45], s[22:23]
	v_pk_mul_f32 v[46:47], v[46:47], s[22:23]
	v_pk_mul_f32 v[48:49], v[48:49], s[22:23]
	v_pk_mul_f32 v[50:51], v[50:51], s[22:23]
	v_pk_mul_f32 v[52:53], v[52:53], s[22:23]
	v_pk_mul_f32 v[54:55], v[54:55], s[22:23]
	v_pk_mul_f32 v[56:57], v[56:57], s[22:23]
	v_pk_mul_f32 v[58:59], v[58:59], s[22:23]
	v_pk_mul_f32 v[60:61], v[60:61], s[22:23]
	v_pk_mul_f32 v[62:63], v[62:63], s[22:23]
	v_pk_mul_f32 v[64:65], v[64:65], s[22:23]
	v_cvt_pk_fp8_f32 v196, v2, v6
	v_cvt_pk_fp8_f32 v197, v18, v22
	v_cvt_pk_fp8_f32 v198, v34, v38
	v_cvt_pk_fp8_f32 v199, v50, v54
	v_cvt_pk_fp8_f32 v196, v10, v14 op_sel:[0,0,1]
	v_cvt_pk_fp8_f32 v197, v26, v30 op_sel:[0,0,1]
	v_cvt_pk_fp8_f32 v198, v42, v46 op_sel:[0,0,1]
	v_cvt_pk_fp8_f32 v199, v58, v62 op_sel:[0,0,1]
	s_nop 0
	global_store_dwordx4 v206, v[196:199], s[8:9] offset:-4096 nt
	v_cvt_pk_fp8_f32 v200, v3, v7
	v_cvt_pk_fp8_f32 v201, v19, v23
	v_cvt_pk_fp8_f32 v202, v35, v39
	v_cvt_pk_fp8_f32 v203, v51, v55
	v_cvt_pk_fp8_f32 v200, v11, v15 op_sel:[0,0,1]
	v_cvt_pk_fp8_f32 v201, v27, v31 op_sel:[0,0,1]
	v_cvt_pk_fp8_f32 v202, v43, v47 op_sel:[0,0,1]
	v_cvt_pk_fp8_f32 v203, v59, v63 op_sel:[0,0,1]
	s_nop 0
	global_store_dwordx4 v206, v[200:203], s[8:9] offset:-2048 nt
	v_cvt_pk_fp8_f32 v196, v4, v8
	v_cvt_pk_fp8_f32 v197, v20, v24
	v_cvt_pk_fp8_f32 v198, v36, v40
	v_cvt_pk_fp8_f32 v199, v52, v56
	v_cvt_pk_fp8_f32 v196, v12, v16 op_sel:[0,0,1]
	v_cvt_pk_fp8_f32 v197, v28, v32 op_sel:[0,0,1]
	v_cvt_pk_fp8_f32 v198, v44, v48 op_sel:[0,0,1]
	v_cvt_pk_fp8_f32 v199, v60, v64 op_sel:[0,0,1]
	s_nop 0
	global_store_dwordx4 v206, v[196:199], s[8:9] offset:0 nt
	v_cvt_pk_fp8_f32 v200, v5, v9
	v_cvt_pk_fp8_f32 v201, v21, v25
	v_cvt_pk_fp8_f32 v202, v37, v41
	v_cvt_pk_fp8_f32 v203, v53, v57
	v_cvt_pk_fp8_f32 v200, v13, v17 op_sel:[0,0,1]
	v_cvt_pk_fp8_f32 v201, v29, v33 op_sel:[0,0,1]
	v_cvt_pk_fp8_f32 v202, v45, v49 op_sel:[0,0,1]
	v_cvt_pk_fp8_f32 v203, v61, v65 op_sel:[0,0,1]
	s_nop 0
	global_store_dwordx4 v206, v[200:203], s[8:9] offset:2048 nt
	s_add_u32 s3, s3, 256
	s_add_u32 s5, s5, 1
	s_cmp_lt_u32 s3, s4
	s_cbranch_scc0 .Lfc3_fin

; __device__ __forceinline__ void item8_load(const float* W, int N, int k0, int n0, int lane, f32x4 (&rg)[16]) {
; #pragma unroll
;     for (int i = 0; i < 16; ++i) rg[i] = __builtin_nontemporal_load((const f32x4*)(W + (size_t)(k0 + 8 * i + (lane >> 3)) * N + n0 + 4 * (lane & 7)));
; }
.Lfc3_scb1:
	s_lshl_b32 s25, s24, 4
	v_mad_u32_u24 v207, v204, s25, v205
	global_load_dwordx4 v[2:5], v207, s[6:7] nt
	s_add_u32 s6, s6, s24
	s_addc_u32 s7, s7, 0
	global_load_dwordx4 v[6:9], v207, s[6:7] nt
	s_add_u32 s6, s6, s24
	s_addc_u32 s7, s7, 0
	global_load_dwordx4 v[10:13], v207, s[6:7] nt
	s_add_u32 s6, s6, s24
	s_addc_u32 s7, s7, 0
	global_load_dwordx4 v[14:17], v207, s[6:7] nt
	s_add_u32 s6, s6, s24
	s_addc_u32 s7, s7, 0
	global_load_dwordx4 v[18:21], v207, s[6:7] nt
	s_add_u32 s6, s6, s24
	s_addc_u32 s7, s7, 0
	global_load_dwordx4 v[22:25], v207, s[6:7] nt
	s_add_u32 s6, s6, s24
	s_addc_u32 s7, s7, 0
	global_load_dwordx4 v[26:29], v207, s[6:7] nt
	s_add_u32 s6, s6, s24
	s_addc_u32 s7, s7, 0
	global_load_dwordx4 v[30:33], v207, s[6:7] nt
	s_add_u32 s6, s6, s24
	s_addc_u32 s7, s7, 0
	global_load_dwordx4 v[34:37], v207, s[6:7] nt
	s_add_u32 s6, s6, s24
	s_addc_u32 s7, s7, 0
	global_load_dwordx4 v[38:41], v207, s[6:7] nt
	s_add_u32 s6, s6, s24
	s_addc_u32 s7, s7, 0
	global_load_dwordx4 v[42:45], v207, s[6:7] nt
	s_add_u32 s6, s6, s24
	s_addc_u32 s7, s7, 0
	global_load_dwordx4 v[46:49], v207, s[6:7] nt
	s_add_u32 s6, s6, s24
	s_addc_u32 s7, s7, 0
	global_load_dwordx4 v[50:53], v207, s[6:7] nt
	s_add_u32 s6, s6, s24
	s_addc_u32 s7, s7, 0
	global_load_dwordx4 v[54:57], v207, s[6:7] nt
	s_add_u32 s6, s6, s24
	s_addc_u32 s7, s7, 0
	global_load_dwordx4 v[58:61], v207, s[6:7] nt
	s_add_u32 s6, s6, s24
	s_addc_u32 s7, s7, 0
	global_load_dwordx4 v[62:65], v207, s[6:7] nt
	s_mov_b32 s26, 53760
	s_add_u32 s29, s3, s26
	s_cmp_lt_u32 s29, 0x10000
	s_cbranch_scc0 .Lfc3_ddb1
	s_lshr_b32 s30, s29, 11
	s_and_b32 s26, s29, 0x7ff
	s_lshr_b32 s31, s26, 7
	s_and_b32 s32, s26, 0x7f
	s_and_b32 s26, s32, 63
	s_lshr_b32 s26, s26, 2
	s_lshl_b32 s26, s26, 8
	s_lshr_b32 s27, s32, 6
	s_lshl_b32 s27, s27, 7
	s_add_u32 s26, s26, s27
	s_and_b32 s27, s32, 3
	s_lshl_b32 s27, s27, 5
	s_add_u32 s26, s26, s27
	s_lshl_b32 s26, s26, 11
	s_lshl_b32 s27, s30, 23
	s_add_u32 s26, s26, s27
	s_lshl_b32 s27, s31, 7
	s_add_u32 s26, s26, s27
	s_add_u32 s26, s26, 0x4001000
	s_branch .Lfc3_dcb1

; #define LAS __attribute__((address_space(3)))
; #define LDS_WAIT() asm volatile("s_waitcnt lgkmcnt(0)" ::: "memory")
; __device__ __forceinline__ void item8_finish(int K, unsigned char* WT, int k0, int r0, LAS float* scr, int lane, const f32x4 (&rg)[16]) {
; #pragma unroll
;     for (int i = 0; i < 16; ++i) { LAS float* d = scr + (8 * i + (lane >> 3)) * 33 + 4 * (lane & 7); d[0] = rg[i].x; d[1] = rg[i].y; d[2] = rg[i].z; d[3] = rg[i].w; }
;     LDS_WAIT();
;     const int c = lane & 7;
; #pragma unroll
;     for (int j = 0; j < 4; ++j) { const int n = (lane >> 3) + 8 * j; const LAS float* sp = scr + (16 * c) * 33 + n; int w[4];
; #pragma unroll
;         for (int q = 0; q < 4; ++q) { w[q] = __builtin_amdgcn_cvt_pk_fp8_f32(sp[(4 * q) * 33] * 256.f, sp[(4 * q + 1) * 33] * 256.f, 0, false); w[q] = __builtin_amdgcn_cvt_pk_fp8_f32(sp[(4 * q + 2) * 33] * 256.f, sp[(4 * q + 3) * 33] * 256.f, w[q], true); }
;         u32x4 o; o.x = (unsigned)w[0]; o.y = (unsigned)w[1]; o.z = (unsigned)w[2]; o.w = (unsigned)w[3];
;         __builtin_nontemporal_store(o, (u32x4*)(WT + (size_t)(r0 + n) * K + k0 + 16 * c)); }
.Lfc3_cv1:
	v_pk_mul_f32 v[66:67], v[66:67], s[22:23]
	v_pk_mul_f32 v[68:69], v[68:69], s[22:23]
	v_pk_mul_f32 v[70:71], v[70:71], s[22:23]
	v_pk_mul_f32 v[72:73], v[72:73], s[22:23]
	v_pk_mul_f32 v[74:75], v[74:75], s[22:23]
	v_pk_mul_f32 v[76:77], v[76:77], s[22:23]
	v_pk_mul_f32 v[78:79], v[78:79], s[22:23]
	v_pk_mul_f32 v[80:81], v[80:81], s[22:23]
	v_pk_mul_f32 v[82:83], v[82:83], s[22:23]
	v_pk_mul_f32 v[84:85], v[84:85], s[22:23]
	v_pk_mul_f32 v[86:87], v[86:87], s[22:23]
	v_pk_mul_f32 v[88:89], v[88:89], s[22:23]
	v_pk_mul_f32 v[90:91], v[90:91], s[22:23]
	v_pk_mul_f32 v[92:93], v[92:93], s[22:23]
	v_pk_mul_f32 v[94:95], v[94:95], s[22:23]
	v_pk_mul_f32 v[96:97], v[96:97], s[22:23]
	v_pk_mul_f32 v[98:99], v[98:99], s[22:23]
	v_pk_mul_f32 v[100:101], v[100:101], s[22:23]
	v_pk_mul_f32 v[102:103], v[102:103], s[22:23]
	v_pk_mul_f32 v[104:105], v[104:105], s[22:23]
	v_pk_mul_f32 v[106:107], v[106:107], s[22:23]
	v_pk_mul_f32 v[108:109], v[108:109], s[22:23]
	v_pk_mul_f32 v[110:111], v[110:111], s[22:23]
	v_pk_mul_f32 v[112:113], v[112:113], s[22:23]
	v_pk_mul_f32 v[114:115], v[114:115], s[22:23]
	v_pk_mul_f32 v[116:117], v[116:117], s[22:23]
	v_pk_mul_f32 v[118:119], v[118:119], s[22:23]
	v_pk_mul_f32 v[120:121], v[120:121], s[22:23]
	v_pk_mul_f32 v[122:123], v[122:123], s[22:23]
	v_pk_mul_f32 v[124:125], v[124:125], s[22:23]
	v_pk_mul_f32 v[126:127], v[126:127], s[22:23]
	v_pk_mul_f32 v[128:129], v[128:129], s[22:23]
	v_cvt_pk_fp8_f32 v196, v66, v70
	v_cvt_pk_fp8_f32 v197, v82, v86
	v_cvt_pk_fp8_f32 v198, v98, v102
	v_cvt_pk_fp8_f32 v199, v114, v118
	v_cvt_pk_fp8_f32 v196, v74, v78 op_sel:[0,0,1]
	v_cvt_pk_fp8_f32 v197, v90, v94 op_sel:[0,0,1]
	v_cvt_pk_fp8_f32 v198, v106, v110 op_sel:[0,0,1]
	v_cvt_pk_fp8_f32 v199, v122, v126 op_sel:[0,0,1]
	s_nop 0
	global_store_dwordx4 v206, v[196:199], s[8:9] offset:-4096 nt
	v_cvt_pk_fp8_f32 v200, v67, v71
	v_cvt_pk_fp8_f32 v201, v83, v87
	v_cvt_pk_fp8_f32 v202, v99, v103
	v_cvt_pk_fp8_f32 v203, v115, v119
	v_cvt_pk_fp8_f32 v200, v75, v79 op_sel:[0,0,1]
	v_cvt_pk_fp8_f32 v201, v91, v95 op_sel:[0,0,1]
	v_cvt_pk_fp8_f32 v202, v107, v111 op_sel:[0,0,1]
	v_cvt_pk_fp8_f32 v203, v123, v127 op_sel:[0,0,1]
	s_nop 0
	global_store_dwordx4 v206, v[200:203], s[8:9] offset:-2048 nt
	v_cvt_pk_fp8_f32 v196, v68, v72
	v_cvt_pk_fp8_f32 v197, v84, v88
	v_cvt_pk_fp8_f32 v198, v100, v104
	v_cvt_pk_fp8_f32 v199, v116, v120
	v_cvt_pk_fp8_f32 v196, v76, v80 op_sel:[0,0,1]
	v_cvt_pk_fp8_f32 v197, v92, v96 op_sel:[0,0,1]
	v_cvt_pk_fp8_f32 v198, v108, v112 op_sel:[0,0,1]
	v_cvt_pk_fp8_f32 v199, v124, v128 op_sel:[0,0,1]
	s_nop 0
	global_store_dwordx4 v206, v[196:199], s[8:9] offset:0 nt
	v_cvt_pk_fp8_f32 v200, v69, v73
	v_cvt_pk_fp8_f32 v201, v85, v89
	v_cvt_pk_fp8_f32 v202, v101, v105
	v_cvt_pk_fp8_f32 v203, v117, v121
	v_cvt_pk_fp8_f32 v200, v77, v81 op_sel:[0,0,1]
	v_cvt_pk_fp8_f32 v201, v93, v97 op_sel:[0,0,1]
	v_cvt_pk_fp8_f32 v202, v109, v113 op_sel:[0,0,1]
	v_cvt_pk_fp8_f32 v203, v125, v129 op_sel:[0,0,1]
	s_nop 0
	global_store_dwordx4 v206, v[200:203], s[8:9] offset:2048 nt
	s_add_u32 s3, s3, 256
	s_add_u32 s5, s5, 1
	s_cmp_lt_u32 s3, s4
	s_cbranch_scc0 .Lfc3_fin

; __device__ __forceinline__ void item8_load(const float* W, int N, int k0, int n0, int lane, f32x4 (&rg)[16]) {
; #pragma unroll
;     for (int i = 0; i < 16; ++i) rg[i] = __builtin_nontemporal_load((const f32x4*)(W + (size_t)(k0 + 8 * i + (lane >> 3)) * N + n0 + 4 * (lane & 7)));
; }
.Lfc3_scb2:
	s_lshl_b32 s25, s24, 4
	v_mad_u32_u24 v207, v204, s25, v205
	global_load_dwordx4 v[66:69], v207, s[6:7] nt
	s_add_u32 s6, s6, s24
	s_addc_u32 s7, s7, 0
	global_load_dwordx4 v[70:73], v207, s[6:7] nt
	s_add_u32 s6, s6, s24
	s_addc_u32 s7, s7, 0
	global_load_dwordx4 v[74:77], v207, s[6:7] nt
	s_add_u32 s6, s6, s24
	s_addc_u32 s7, s7, 0
	global_load_dwordx4 v[78:81], v207, s[6:7] nt
	s_add_u32 s6, s6, s24
	s_addc_u32 s7, s7, 0
	global_load_dwordx4 v[82:85], v207, s[6:7] nt
	s_add_u32 s6, s6, s24
	s_addc_u32 s7, s7, 0
	global_load_dwordx4 v[86:89], v207, s[6:7] nt
	s_add_u32 s6, s6, s24
	s_addc_u32 s7, s7, 0
	global_load_dwordx4 v[90:93], v207, s[6:7] nt
	s_add_u32 s6, s6, s24
	s_addc_u32 s7, s7, 0
	global_load_dwordx4 v[94:97], v207, s[6:7] nt
	s_add_u32 s6, s6, s24
	s_addc_u32 s7, s7, 0
	global_load_dwordx4 v[98:101], v207, s[6:7] nt
	s_add_u32 s6, s6, s24
	s_addc_u32 s7, s7, 0
	global_load_dwordx4 v[102:105], v207, s[6:7] nt
	s_add_u32 s6, s6, s24
	s_addc_u32 s7, s7, 0
	global_load_dwordx4 v[106:109], v207, s[6:7] nt
	s_add_u32 s6, s6, s24
	s_addc_u32 s7, s7, 0
	global_load_dwordx4 v[110:113], v207, s[6:7] nt
	s_add_u32 s6, s6, s24
	s_addc_u32 s7, s7, 0
	global_load_dwordx4 v[114:117], v207, s[6:7] nt
	s_add_u32 s6, s6, s24
	s_addc_u32 s7, s7, 0
	global_load_dwordx4 v[118:121], v207, s[6:7] nt
	s_add_u32 s6, s6, s24
	s_addc_u32 s7, s7, 0
	global_load_dwordx4 v[122:125], v207, s[6:7] nt
	s_add_u32 s6, s6, s24
	s_addc_u32 s7, s7, 0
	global_load_dwordx4 v[126:129], v207, s[6:7] nt
	s_mov_b32 s26, 53760
	s_add_u32 s29, s3, s26
	s_cmp_lt_u32 s29, 0x10000
	s_cbranch_scc0 .Lfc3_ddb2
	s_lshr_b32 s30, s29, 11
	s_and_b32 s26, s29, 0x7ff
	s_lshr_b32 s31, s26, 7
	s_and_b32 s32, s26, 0x7f
	s_and_b32 s26, s32, 63
	s_lshr_b32 s26, s26, 2
	s_lshl_b32 s26, s26, 8
	s_lshr_b32 s27, s32, 6
	s_lshl_b32 s27, s27, 7
	s_add_u32 s26, s26, s27
	s_and_b32 s27, s32, 3
	s_lshl_b32 s27, s27, 5
	s_add_u32 s26, s26, s27
	s_lshl_b32 s26, s26, 11
	s_lshl_b32 s27, s30, 23
	s_add_u32 s26, s26, s27
	s_lshl_b32 s27, s31, 7
	s_add_u32 s26, s26, s27
	s_add_u32 s26, s26, 0x4001000
	s_branch .Lfc3_dcb2

; #define LAS __attribute__((address_space(3)))
; #define LDS_WAIT() asm volatile("s_waitcnt lgkmcnt(0)" ::: "memory")
; __device__ __forceinline__ void item8_finish(int K, unsigned char* WT, int k0, int r0, LAS float* scr, int lane, const f32x4 (&rg)[16]) {
; #pragma unroll
;     for (int i = 0; i < 16; ++i) { LAS float* d = scr + (8 * i + (lane >> 3)) * 33 + 4 * (lane & 7); d[0] = rg[i].x; d[1] = rg[i].y; d[2] = rg[i].z; d[3] = rg[i].w; }
;     LDS_WAIT();
;     const int c = lane & 7;
; #pragma unroll
;     for (int j = 0; j < 4; ++j) { const int n = (lane >> 3) + 8 * j; const LAS float* sp = scr + (16 * c) * 33 + n; int w[4];
; #pragma unroll
;         for (int q = 0; q < 4; ++q) { w[q] = __builtin_amdgcn_cvt_pk_fp8_f32(sp[(4 * q) * 33] * 256.f, sp[(4 * q + 1) * 33] * 256.f, 0, false); w[q] = __builtin_amdgcn_cvt_pk_fp8_f32(sp[(4 * q + 2) * 33] * 256.f, sp[(4 * q + 3) * 33] * 256.f, w[q], true); }
;         u32x4 o; o.x = (unsigned)w[0]; o.y = (unsigned)w[1]; o.z = (unsigned)w[2]; o.w = (unsigned)w[3];
;         __builtin_nontemporal_store(o, (u32x4*)(WT + (size_t)(r0 + n) * K + k0 + 16 * c)); }
.Lfc3_cv2:
	v_pk_mul_f32 v[130:131], v[130:131], s[22:23]
	v_pk_mul_f32 v[132:133], v[132:133], s[22:23]
	v_pk_mul_f32 v[134:135], v[134:135], s[22:23]
	v_pk_mul_f32 v[136:137], v[136:137], s[22:23]
	v_pk_mul_f32 v[138:139], v[138:139], s[22:23]
	v_pk_mul_f32 v[140:141], v[140:141], s[22:23]
	v_pk_mul_f32 v[142:143], v[142:143], s[22:23]
	v_pk_mul_f32 v[144:145], v[144:145], s[22:23]
	v_pk_mul_f32 v[146:147], v[146:147], s[22:23]
	v_pk_mul_f32 v[148:149], v[148:149], s[22:23]
	v_pk_mul_f32 v[150:151], v[150:151], s[22:23]
	v_pk_mul_f32 v[152:153], v[152:153], s[22:23]
	v_pk_mul_f32 v[154:155], v[154:155], s[22:23]
	v_pk_mul_f32 v[156:157], v[156:157], s[22:23]
	v_pk_mul_f32 v[158:159], v[158:159], s[22:23]
	v_pk_mul_f32 v[160:161], v[160:161], s[22:23]
	v_pk_mul_f32 v[162:163], v[162:163], s[22:23]
	v_pk_mul_f32 v[164:165], v[164:165], s[22:23]
	v_pk_mul_f32 v[166:167], v[166:167], s[22:23]
	v_pk_mul_f32 v[168:169], v[168:169], s[22:23]
	v_pk_mul_f32 v[170:171], v[170:171], s[22:23]
	v_pk_mul_f32 v[172:173], v[172:173], s[22:23]
	v_pk_mul_f32 v[174:175], v[174:175], s[22:23]
	v_pk_mul_f32 v[176:177], v[176:177], s[22:23]
	v_pk_mul_f32 v[178:179], v[178:179], s[22:23]
	v_pk_mul_f32 v[180:181], v[180:181], s[22:23]
	v_pk_mul_f32 v[182:183], v[182:183], s[22:23]
	v_pk_mul_f32 v[184:185], v[184:185], s[22:23]
	v_pk_mul_f32 v[186:187], v[186:187], s[22:23]
	v_pk_mul_f32 v[188:189], v[188:189], s[22:23]
	v_pk_mul_f32 v[190:191], v[190:191], s[22:23]
	v_pk_mul_f32 v[192:193], v[192:193], s[22:23]
	v_cvt_pk_fp8_f32 v196, v130, v134
	v_cvt_pk_fp8_f32 v197, v146, v150
	v_cvt_pk_fp8_f32 v198, v162, v166
	v_cvt_pk_fp8_f32 v199, v178, v182
	v_cvt_pk_fp8_f32 v196, v138, v142 op_sel:[0,0,1]
	v_cvt_pk_fp8_f32 v197, v154, v158 op_sel:[0,0,1]
	v_cvt_pk_fp8_f32 v198, v170, v174 op_sel:[0,0,1]
	v_cvt_pk_fp8_f32 v199, v186, v190 op_sel:[0,0,1]
	s_nop 0
	global_store_dwordx4 v206, v[196:199], s[8:9] offset:-4096 nt
	v_cvt_pk_fp8_f32 v200, v131, v135
	v_cvt_pk_fp8_f32 v201, v147, v151
	v_cvt_pk_fp8_f32 v202, v163, v167
	v_cvt_pk_fp8_f32 v203, v179, v183
	v_cvt_pk_fp8_f32 v200, v139, v143 op_sel:[0,0,1]
	v_cvt_pk_fp8_f32 v201, v155, v159 op_sel:[0,0,1]
	v_cvt_pk_fp8_f32 v202, v171, v175 op_sel:[0,0,1]
	v_cvt_pk_fp8_f32 v203, v187, v191 op_sel:[0,0,1]
	s_nop 0
	global_store_dwordx4 v206, v[200:203], s[8:9] offset:-2048 nt
	v_cvt_pk_fp8_f32 v196, v132, v136
	v_cvt_pk_fp8_f32 v197, v148, v152
	v_cvt_pk_fp8_f32 v198, v164, v168
	v_cvt_pk_fp8_f32 v199, v180, v184
	v_cvt_pk_fp8_f32 v196, v140, v144 op_sel:[0,0,1]
	v_cvt_pk_fp8_f32 v197, v156, v160 op_sel:[0,0,1]
	v_cvt_pk_fp8_f32 v198, v172, v176 op_sel:[0,0,1]
	v_cvt_pk_fp8_f32 v199, v188, v192 op_sel:[0,0,1]
	s_nop 0
	global_store_dwordx4 v206, v[196:199], s[8:9] offset:0 nt
	v_cvt_pk_fp8_f32 v200, v133, v137
	v_cvt_pk_fp8_f32 v201, v149, v153
	v_cvt_pk_fp8_f32 v202, v165, v169
	v_cvt_pk_fp8_f32 v203, v181, v185
	v_cvt_pk_fp8_f32 v200, v141, v145 op_sel:[0,0,1]
	v_cvt_pk_fp8_f32 v201, v157, v161 op_sel:[0,0,1]
	v_cvt_pk_fp8_f32 v202, v173, v177 op_sel:[0,0,1]
	v_cvt_pk_fp8_f32 v203, v189, v193 op_sel:[0,0,1]
	s_nop 0
	global_store_dwordx4 v206, v[200:203], s[8:9] offset:2048 nt
	s_add_u32 s3, s3, 256
	s_add_u32 s5, s5, 1
	s_cmp_lt_u32 s3, s4
	s_cbranch_scc1 .Lfc3_body0

; __global__ void __launch_bounds__(NTHREADS, 2) fwd(Args args) {
;     ...
;         for (int u = bid; u < NBATCH * 68 * 4; u += G) {
;             const int h = u & 3, bc = u >> 2, b = bc / 68, c = bc % 68; const bool lat = c >= 4;
;             const int row0 = lat ? b * SEQ + (c - 4) * 64 : T + b * CTX + c * 64;
;             const int d = tid & 127, tq = tid >> 7;
;             const f32x4 lr4 = *(const f32x4*)(LR + (size_t)(row0 + (tid >> 3)) * 32 + (tid & 7) * 4);
;             u32x4 vraw[4];
; #pragma unroll
;             for (int i = 0; i < 4; ++i) { const int ch = tid + 512 * i, sx = ch & 63, e8 = ch >> 6; vraw[i] = *(const u32x4*)(P + (size_t)(row0 + sx) * NP + C_VG + h * 256 + e8 * 8); }
;             u32x4 qk4[4];
; #pragma unroll
;             for (int i = 0; i < 2; ++i) { const int ch = tid + 512 * i, t = ch >> 4, c16 = ch & 15; const bf16* pr = P + (size_t)(row0 + t) * NP + h * 128 + c16 * 8; qk4[i] = *(const u32x4*)(pr + C_Q); qk4[2 + i] = *(const u32x4*)(pr + C_K); }
.Lfc3_done:
	v_readlane_b32 s4, v247, 0
	v_readlane_b32 s5, v247, 1
	s_nop 3
	s_branch .LBB0_370
.Lfc3_skip:
	s_waitcnt vmcnt(0)
	v_lshrrev_b32_e32 v5, 7, v0
	v_and_b32_e32 v102, 0x7f, v0
	v_mul_u32_u24_e32 v30, 0x880, v5
	v_or_b32_e32 v30, v30, v102
	v_lshlrev_b32_e32 v30, 1, v30
	s_add_i32 s2, 0, 0x16400
	s_add_i32 s3, 0, 0x1a800
	v_add_u32_e32 v31, 0x110, v30
	v_add_u32_e32 v132, s2, v31
	v_add_u32_e32 v133, s3, v31
	v_add_u32_e32 v31, 0x220, v30
	v_add_u32_e32 v134, s2, v31
	v_add_u32_e32 v135, s3, v31
	v_add_u32_e32 v31, 0x330, v30
	s_movk_i32 s0, 0x180
	v_add_u32_e32 v136, s2, v31
	v_add_u32_e32 v137, s3, v31
	v_add_u32_e32 v31, 0x440, v30
	v_cmp_gt_u32_e64 s[6:7], s0, v0
	s_movk_i32 s0, 0x100
	v_add_u32_e32 v138, s2, v31
	v_add_u32_e32 v139, s3, v31
	v_add_u32_e32 v31, 0x550, v30
	v_writelane_b32 v246, s4, 32
	v_and_b32_e32 v2, 28, v194
	v_cmp_gt_u32_e64 s[8:9], s0, v0
	s_movk_i32 s0, 0x80
	v_add_u32_e32 v140, s2, v31
	v_add_u32_e32 v141, s3, v31
	v_add_u32_e32 v31, 0x660, v30
	v_writelane_b32 v246, s5, 33
	v_lshlrev_b32_e32 v38, 2, v2
	v_mov_b32_e32 v39, 0
	v_lshlrev_b32_e32 v4, 4, v0
	v_cmp_gt_u32_e64 s[10:11], s0, v0
	s_movk_i32 s0, 0xff
	v_add_u32_e32 v142, s2, v31
	v_add_u32_e32 v143, s3, v31
	v_add_u32_e32 v31, 0x770, v30
	v_lshl_add_u64 v[40:41], s[12:13], 0, v[38:39]
	v_and_b32_e32 v2, 0xf0, v4
	v_mov_b32_e32 v3, v39
	v_cmp_lt_u32_e64 s[12:13], s0, v0
	s_movk_i32 s0, 0x17f
	v_readlane_b32 s16, v246, 21
	v_add_u32_e32 v144, s2, v31
	v_add_u32_e32 v145, s3, v31
	v_add_u32_e32 v31, 0x880, v30
	v_lshl_add_u64 v[42:43], s[62:63], 0, v[2:3]
	v_add_u32_e32 v7, s2, v2
	v_add_u32_e32 v9, s3, v2
	v_and_b32_e32 v2, 0x70, v4
	v_cmp_lt_u32_e64 s[14:15], s0, v0
	s_lshl_b32 s0, s16, 1
	v_add_u32_e32 v146, s2, v31
	v_add_u32_e32 v147, s3, v31
	v_add_u32_e32 v31, 0x990, v30
	v_add_u32_e32 v11, 0, v2
	v_and_b32_e32 v2, 0xe0, v4
	s_and_b32 s4, s0, 2
	s_lshr_b32 s0, s51, 3
	v_add_u32_e32 v148, s2, v31
	v_add_u32_e32 v149, s3, v31
	v_add_u32_e32 v31, 0xaa0, v30
	v_lshrrev_b32_e32 v103, 3, v0
	v_add_u32_e32 v13, 0, v2
	v_and_b32_e32 v15, 15, v0
	s_and_b32 s5, s0, 0x1ffffff0
	v_and_b32_e32 v2, 48, v220
	v_add_u32_e32 v150, s2, v31
	v_add_u32_e32 v151, s3, v31
	v_add_u32_e32 v31, 0xbb0, v30
	v_lshlrev_b32_e32 v3, 7, v103
	v_or_b32_e32 v4, s5, v15
	v_add_u32_e32 v2, 0, v2
	s_movk_i32 s0, 0x110
	v_add_u32_e32 v152, s2, v31
	v_add_u32_e32 v153, s3, v31
	v_add_u32_e32 v31, 0xcc0, v30
	v_mad_u64_u32 v[44:45], s[0:1], v4, s0, v[2:3]
	v_add_u32_e32 v154, s2, v31
	v_add_u32_e32 v155, s3, v31
	v_add_u32_e32 v31, 0xdd0, v30
	v_and_b32_e32 v14, 4, v194
	v_or_b32_e32 v22, 0x200, v0
	v_lshrrev_b32_e32 v45, 4, v0
	v_add_u32_e32 v156, s2, v31
	v_add_u32_e32 v157, s3, v31
	v_add_u32_e32 v31, 0xee0, v30
	v_lshrrev_b32_e32 v4, 2, v220
	v_lshrrev_b32_e32 v107, 4, v22
	v_add_u32_e32 v130, s2, v30
	v_add_u32_e32 v131, s3, v30
	v_add_u32_e32 v158, s2, v31
	v_add_u32_e32 v159, s3, v31
	v_add_u32_e32 v31, 0xff0, v30
	v_add_u32_e32 v162, 0, v30
	v_mul_u32_u24_e32 v30, 0x110, v45
	v_lshlrev_b32_e32 v14, 1, v14
	v_and_b32_e32 v16, 12, v4
	v_writelane_b32 v246, s51, 34
	v_add3_u32 v163, v13, v30, v14
	v_mul_u32_u24_e32 v30, 0x110, v107
	s_lshl_b32 s0, s16, 3
	v_writelane_b32 v246, s68, 35
	v_add3_u32 v164, v13, v30, v14
	v_lshl_or_b32 v13, s4, 4, v15
	v_or_b32_e32 v16, s5, v16
	s_and_b32 s0, s0, 0xffffff0
	v_lshrrev_b32_e32 v4, 2, v0
	v_writelane_b32 v246, s69, 36
	v_add_u32_e32 v160, s2, v31
	v_add_u32_e32 v161, s3, v31
	v_cmp_lt_u32_e64 s[2:3], v13, v16
	v_and_or_b32 v17, v4, 12, s0
	v_and_b32_e32 v4, 48, v0
	v_or_b32_e32 v32, 3, v16
	v_writelane_b32 v246, s2, 30
	v_add_u32_e32 v19, 0, v4
	s_and_b32 s0, s51, 0xffffffc0
	v_lshrrev_b32_e32 v4, 1, v0
	v_writelane_b32 v246, s3, 31
	v_cmp_lt_u32_e64 s[2:3], v13, v32
	v_and_b32_e32 v4, 24, v4
	s_add_i32 s0, s0, 0
	v_or_b32_e32 v33, 2, v16
	v_writelane_b32 v246, s2, 37
	s_lshl_b32 s1, s4, 5
	v_lshl_or_b32 v18, s16, 5, v15
	v_add_u32_e32 v20, s0, v4
	s_movk_i32 s0, 0x90
	v_or_b32_e32 v30, 16, v13
	v_writelane_b32 v246, s3, 38
	v_cmp_lt_u32_e64 s[2:3], v13, v33
	s_add_i32 s1, s1, 0
	s_ashr_i32 s95, s94, 31
	v_lshlrev_b32_e32 v12, 2, v102
	v_or_b32_e32 v31, 1, v16
	v_cmp_lt_u32_e64 s[16:17], v16, v13
	v_writelane_b32 v246, s2, 39
	v_cmp_lt_u32_e64 s[24:25], v16, v30
	v_cmp_lt_u32_e64 s[26:27], v30, v16
	v_lshl_add_u32 v16, v15, 1, s1
	v_mul_lo_u32 v17, v17, s0
	v_mul_lo_u32 v18, v18, s0
	s_lshl_b64 s[0:1], s[94:95], 9
	v_lshl_add_u32 v105, v5, 11, 0
	v_add_u32_e32 v106, 0, v12
	v_writelane_b32 v246, s3, 40
	v_or_b32_e32 v48, s0, v12
	s_lshl_b64 s[2:3], s[94:95], 14
	v_lshlrev_b32_e32 v12, 7, v102
	v_lshlrev_b32_e32 v5, 5, v5
	v_mul_u32_u24_e32 v28, 0x88, v45
	v_or3_b32 v50, s2, v12, v5
	v_and_b32_e32 v5, 7, v0
	v_lshlrev_b32_e32 v28, 1, v28
	s_lshl_b64 s[4:5], s[94:95], 15
; #define LAS __attribute__((address_space(3)))
; __global__ void __launch_bounds__(NTHREADS, 2) fwd(Args args) {
;     ...
;         for (int u = bid; u < NBATCH * 68 * 4; u += G) {
;             const int h = u & 3, bc = u >> 2, b = bc / 68, c = bc % 68; const bool lat = c >= 4;
;             const int row0 = lat ? b * SEQ + (c - 4) * 64 : T + b * CTX + c * 64;
;             const int d = tid & 127, tq = tid >> 7;
;             const f32x4 lr4 = *(const f32x4*)(LR + (size_t)(row0 + (tid >> 3)) * 32 + (tid & 7) * 4);
;             u32x4 vraw[4];
; #pragma unroll
;             for (int i = 0; i < 4; ++i) { const int ch = tid + 512 * i, sx = ch & 63, e8 = ch >> 6; vraw[i] = *(const u32x4*)(P + (size_t)(row0 + sx) * NP + C_VG + h * 256 + e8 * 8); }
;             u32x4 qk4[4];
; #pragma unroll
;             for (int i = 0; i < 2; ++i) { const int ch = tid + 512 * i, t = ch >> 4, c16 = ch & 15; const bf16* pr = P + (size_t)(row0 + t) * NP + h * 128 + c16 * 8; qk4[i] = *(const u32x4*)(pr + C_Q); qk4[2 + i] = *(const u32x4*)(pr + C_K); }
;             if (h != hprev) { hprev = h;
; #pragma unroll
;                 for (int r = 0; r < 16; ++r) { wg[0][r] = wgk_f[r * 512 + h * 128 + d]; wg[1][r] = wgk_b[r * 512 + h * 128 + d]; }
;                 bias2[0] = bgk_f[h * 128 + d]; bias2[1] = bgk_b[h * 128 + d]; }
;             *(LAS f32x4*)(LRs + (tid >> 3) * 32 + (tid & 7) * 4) = lr4;
; #pragma unroll
;             for (int i = 0; i < 2; ++i) { const int ch = tid + 512 * i, t = ch >> 4, c16 = ch & 15; *(LAS u32x4*)(Qs + t * 136 + c16 * 8) = qk4[i]; *(LAS u32x4*)(Ks + t * 136 + c16 * 8) = qk4[2 + i]; }
; #pragma unroll
;             for (int i = 0; i < 4; ++i) { const int ch = tid + 512 * i, sx = ch & 63, e8 = ch >> 6; const unsigned ww[4] = {vraw[i].x, vraw[i].y, vraw[i].z, vraw[i].w};
; #pragma unroll
;                 for (int j = 0; j < 4; ++j) { VTs[(e8 * 8 + 2 * j) * 72 + sx] = (bf16)(ww[j] & 0xffffu); VTs[(e8 * 8 + 2 * j + 1) * 72 + sx] = (bf16)(ww[j] >> 16); } }
	v_lshlrev_b32_e32 v5, 4, v5
	v_and_b32_e32 v4, 31, v0
	v_add_u32_e32 v122, v7, v28
	v_add_u32_e32 v123, v9, v28
	v_mul_u32_u24_e32 v28, 0x88, v107
	v_mul_u32_u24_e32 v14, 0x110, v13
	v_cmp_gt_u32_e64 s[34:35], v13, v32
	v_cmp_gt_u32_e64 s[36:37], v13, v33
	v_cmp_gt_u32_e64 s[38:39], v13, v31
	v_or3_b32 v12, s4, v3, v5
	v_mov_b32_e32 v13, s5
	s_mov_b64 s[18:19], 0x68200000
	v_add3_u32 v104, 0, v3, v38
	v_lshlrev_b32_e32 v38, 4, v4
	v_and_b32_e32 v4, 56, v103
	v_lshrrev_b32_e32 v23, 3, v22
	v_or_b32_e32 v24, 0x400, v0
	v_or_b32_e32 v26, 0x600, v0
	v_lshlrev_b32_e32 v28, 1, v28
	v_lshl_add_u64 v[52:53], v[12:13], 0, s[18:19]
	v_lshlrev_b32_e32 v3, 8, v45
	v_lshlrev_b32_e32 v12, 4, v15
	v_and_b32_e32 v6, 0x78, v23
	v_lshrrev_b32_e32 v25, 3, v24
	v_lshrrev_b32_e32 v27, 3, v26
	v_add_u32_e32 v124, v7, v28
	v_add_u32_e32 v125, v9, v28
	v_mul_u32_u24_e32 v7, 0x90, v4
	v_lshlrev_b32_e32 v9, 1, v220
	v_mov_b32_e32 v49, s1
	v_readlane_b32 s0, v246, 10
	v_or3_b32 v54, s2, v3, v12
	v_lshlrev_b32_e32 v3, 8, v107
	v_and_b32_e32 v8, 0xb8, v25
	v_add3_u32 v126, 0, v7, v9
	v_mul_u32_u24_e32 v7, 0x90, v6
	s_mov_b32 s46, s0
	v_or3_b32 v56, s2, v3, v12
	v_lshlrev_b32_e32 v3, 7, v27
	v_and_b32_e32 v10, 0xf8, v27
	v_add3_u32 v127, 0, v7, v9
	v_mul_u32_u24_e32 v7, 0x90, v8
	s_mov_b32 s20, s46
	v_or3_b32 v12, s4, v3, v5
	v_lshlrev_b32_e32 v3, 7, v25
	v_add3_u32 v128, 0, v7, v9
	v_mul_u32_u24_e32 v7, 0x90, v10
	v_lshrrev_b32_e32 v165, 5, v0
	v_lshrrev_b32_e32 v166, 5, v22
	v_lshrrev_b32_e32 v167, 5, v24
	v_lshrrev_b32_e32 v168, 5, v26
	v_readlane_b32 s1, v246, 11
	s_ashr_i32 s47, s0, 31
	s_mov_b32 s48, s94
	v_writelane_b32 v246, s20, 10
	v_lshl_add_u64 v[58:59], v[12:13], 0, s[18:19]
	v_or3_b32 v12, s4, v3, v5
	v_lshlrev_b32_e32 v3, 7, v23
	v_add_u32_e32 v21, 0, v38
	v_lshl_add_u64 v[46:47], s[68:69], 0, v[38:39]
	v_add3_u32 v129, 0, v7, v9
	v_mul_u32_u24_e32 v7, 0x90, v103
	v_mul_u32_u24_e32 v9, 0x90, v23
	v_mul_u32_u24_e32 v28, 0x90, v25
	v_mul_u32_u24_e32 v29, 0x90, v27
	v_mul_u32_u24_e32 v34, 0x110, v30
	v_mul_u32_u24_e32 v35, 0x90, v15
	v_mul_u32_u24_e32 v36, 0x208, v15
	v_mul_u32_u24_e32 v37, 0x208, v165
	v_mul_u32_u24_e32 v22, 0x208, v166
	v_mul_u32_u24_e32 v24, 0x208, v167
	v_mul_u32_u24_e32 v26, 0x208, v168
	v_readlane_b32 s46, v246, 23
	s_nop 3
	s_lshl_b64 s[68:69], s[46:47], 9
	s_lshl_b64 s[0:1], s[46:47], 14
	v_writelane_b32 v246, s21, 11
	s_lshl_b64 s[94:95], s[46:47], 15
	v_lshl_add_u64 v[60:61], v[12:13], 0, s[18:19]
	v_or3_b32 v12, s4, v3, v5
	s_movk_i32 s5, 0x2800
	s_mov_b32 s46, s48
	s_mov_b32 s57, 0
	v_or_b32_e32 v108, 0x400, v102
	v_or_b32_e32 v109, 0x600, v102
	v_or_b32_e32 v110, 0x800, v102
	v_or_b32_e32 v111, 0xa00, v102
	v_or_b32_e32 v112, 0xc00, v102
	v_or_b32_e32 v113, 0xe00, v102
	v_or_b32_e32 v114, 0x1000, v102
	v_or_b32_e32 v115, 0x1200, v102
	v_or_b32_e32 v116, 0x1400, v102
	v_or_b32_e32 v117, 0x1600, v102
	v_or_b32_e32 v118, 0x1800, v102
	v_or_b32_e32 v119, 0x1a00, v102
	v_or_b32_e32 v120, 0x1c00, v102
	v_or_b32_e32 v121, 0x1e00, v102
	v_cmp_lt_u32_e64 s[28:29], v30, v32
	v_cmp_lt_u32_e64 s[30:31], v30, v33
	v_cmp_gt_u32_e64 s[40:41], v30, v32
	v_cmp_gt_u32_e64 s[42:43], v30, v33
	v_cmp_gt_u32_e64 s[44:45], v30, v31
	v_mov_b32_e32 v51, s3
	v_mov_b32_e32 v55, s3
	v_mov_b32_e32 v57, s3
	v_lshl_add_u64 v[62:63], v[12:13], 0, s[18:19]
	s_mov_b32 s20, -1
	v_lshlrev_b32_e32 v38, 1, v4
	v_lshlrev_b32_e32 v64, 1, v6
	v_lshlrev_b32_e32 v66, 1, v8
	v_lshlrev_b32_e32 v68, 1, v10
	v_add_u32_e32 v169, v11, v7
	v_add_u32_e32 v170, v11, v9
	v_add_u32_e32 v171, v11, v28
	v_add_u32_e32 v172, v11, v29
	s_mov_b32 s51, 0xbfb8aa3b
	s_mov_b32 s3, 0x800000
	s_mov_b32 s2, 0x3f317217
	s_mov_b32 s33, 0x7f800000
	s_mov_b32 s4, 0x3d800000
	s_mov_b32 s18, 0xffff
	s_mov_b32 s23, 0xc2ce8ed0
	v_add_u32_e32 v173, v2, v34
	v_add_u32_e32 v174, v16, v17
	v_add_u32_e32 v175, v19, v18
	v_add_u32_e32 v176, v19, v35
	v_add_u32_e32 v177, v20, v36
	v_add3_u32 v178, v21, v37, s5
	v_add3_u32 v179, v21, v22, s5
	v_add3_u32 v180, v21, v24, s5
	v_add3_u32 v181, v21, v26, s5
	v_mov_b32_e32 v182, 0x41b17218
	v_mov_b32_e32 v183, 0x7f800000
	v_add_u32_e32 v184, v2, v14
	v_writelane_b32 v246, s46, 41
	s_mov_b32 s19, s48
	s_nop 0
	v_writelane_b32 v246, s47, 42
	s_branch .LBB0_353
.LBB0_352:
	s_waitcnt lgkmcnt(0)
	s_barrier
	v_readlane_b32 s46, v246, 23
	s_add_i32 s19, s19, s46
	v_lshl_add_u64 v[48:49], v[48:49], 0, s[68:69]
	v_lshl_add_u64 v[50:51], v[50:51], 0, s[0:1]
	v_lshl_add_u64 v[52:53], v[52:53], 0, s[94:95]
	v_lshl_add_u64 v[54:55], v[54:55], 0, s[0:1]
	v_lshl_add_u64 v[56:57], v[56:57], 0, s[0:1]
	v_lshl_add_u64 v[58:59], v[58:59], 0, s[94:95]
	v_lshl_add_u64 v[60:61], v[60:61], 0, s[94:95]
	s_cmpk_lt_i32 s19, 0x440
	v_lshl_add_u64 v[62:63], v[62:63], 0, s[94:95]
	v_readlane_b32 s47, v246, 11
	s_cbranch_scc0 .LBB0_369

; #define MOE_LOAD(r_, RG) do { int rr_ = (r_); \
;         if (rr_ < 65536) { const int e_ = rr_ / 2048, q_ = rr_ % 2048; item8_load(w_gu + (size_t)e_ * 2048 * 4096, 4096, 128 * (q_ / 128), 32 * (q_ % 128), lane, RG); } \
;         else { rr_ -= 65536; const int e_ = rr_ / 1024, q_ = rr_ % 1024; item8_load(w_dn + (size_t)e_ * 2048 * 2048, D, 128 * (q_ / 64), 32 * (q_ % 64), lane, RG); } } while (0)
; __global__ void __launch_bounds__(NTHREADS, 2) fwd(Args args) {
;     ...
;     if (IN(3) && IN(4)) xcd_barrier_bg(bar, [&]() {
;         for (int sl_ = bid * 7 + wave - 1; sl_ < CVBG / 6; sl_ += G * 7) { const int it_ = CV_P0 - CVBG + 2 * (CVBG / 6) + sl_; f32x4 rg_[16]; MOE_LOAD(it_, rg_); MOE_FIN(it_, rg_); }
;         if (bid >= 64) for (int sl_ = (bid - 64) * 7 + wave - 1; sl_ < CVSK; sl_ += (G - 64) * 7) { const int it_ = CV_P0 - CVBG - CVSK + sl_; f32x4 rg_[16]; MOE_LOAD(it_, rg_); MOE_FIN(it_, rg_); } });
.LBB0_376:
	s_cmp_gt_i32 s94, 0xbf
	s_cbranch_scc0 .LBB0_380
	s_addk_i32 s2, 0xfabf
	s_cmpk_gt_i32 s2, 0x53f
	s_cbranch_scc1 .LBB0_380
	v_readlane_b32 s3, v246, 21
	s_mulk_i32 s3, 0x4200
	v_lshlrev_b32_e32 v5, 4, v0
	v_lshrrev_b32_e32 v22, 3, v220
	v_and_b32_e32 v2, 28, v194
	s_add_i32 s3, s3, 0
	v_and_b32_e32 v18, 0x70, v5
	v_lshl_add_u32 v3, v2, 2, s3
	v_mul_u32_u24_e32 v4, 0x84, v22
	v_mul_u32_u24_e32 v5, 0x84, v18
	v_lshlrev_b32_e32 v6, 2, v22
	v_readlane_b32 s8, v246, 10
	v_mov_b32_e32 v19, 0
	v_add3_u32 v26, s3, v5, v6
	s_mul_i32 s3, s8, 7
	v_add_u32_e32 v27, v3, v4
	v_or_b32_e32 v23, 8, v22
	v_or_b32_e32 v24, 16, v22
	v_or_b32_e32 v25, 24, v22
	s_addk_i32 s3, 0xfac0
	v_lshlrev_b32_e32 v20, 2, v2
	v_mov_b32_e32 v21, v19
	v_add_u32_e32 v28, 0x420, v27
	v_add_u32_e32 v29, 0x428, v27
	v_add_u32_e32 v30, 0x840, v27
	v_add_u32_e32 v31, 0x848, v27
	v_add_u32_e32 v32, 0xc60, v27
	v_add_u32_e32 v33, 0xc68, v27
	v_add_u32_e32 v34, 0x1080, v27
	v_add_u32_e32 v35, 0x1088, v27
	v_add_u32_e32 v36, 0x14a0, v27
	v_add_u32_e32 v37, 0x14a8, v27
	v_add_u32_e32 v38, 0x18c0, v27
	v_add_u32_e32 v39, 0x18c8, v27
	v_add_u32_e32 v40, 0x1ce0, v27
	v_add_u32_e32 v41, 0x1ce8, v27
	v_add_u32_e32 v42, 0x2100, v27
	v_add_u32_e32 v43, 0x2108, v27
	v_add_u32_e32 v44, 0x2520, v27
	v_add_u32_e32 v45, 0x2528, v27
	v_add_u32_e32 v46, 0x2940, v27
	v_add_u32_e32 v47, 0x2948, v27
	v_add_u32_e32 v48, 0x2d60, v27
	v_add_u32_e32 v49, 0x2d68, v27
	v_add_u32_e32 v50, 0x3180, v27
	v_add_u32_e32 v51, 0x3188, v27
	v_add_u32_e32 v52, 0x35a0, v27
	v_add_u32_e32 v53, 0x35a8, v27
	v_add_u32_e32 v54, 0x39c0, v27
	v_add_u32_e32 v55, 0x39c8, v27
	v_add_u32_e32 v56, 0x3de0, v27
	v_add_u32_e32 v57, 0x3de8, v27
	v_add_u32_e32 v58, 0x400, v26
	v_add_u32_e32 v59, 0x600, v26
	v_readlane_b32 s9, v246, 11

; #define MOE_RANGE(first_, end_, stride_) do { f32x4 rgA_[16], rgB_[16]; int ia_ = (first_); if (ia_ < (end_)) MOE_LOAD(ia_, rgA_); \
;         while (ia_ < (end_)) { const int ib_ = ia_ + (stride_); if (ib_ < (end_)) MOE_LOAD(ib_, rgB_); MOE_FIN(ia_, rgA_); if (ib_ >= (end_)) break; \
;             ia_ = ib_ + (stride_); if (ia_ < (end_)) MOE_LOAD(ia_, rgA_); MOE_FIN(ib_, rgB_); } } while (0)
; __global__ void __launch_bounds__(NTHREADS, 2) fwd(Args args) {
;     ...
;             if (bid >= 64 + NCMB && wave < 6) MOE_RANGE(CV_P0 + CV2 + CV2X + CV3 + (bid - 64 - NCMB) * 6 + wave, CV_P0 + CV2 + CV2X + CV3 + CV4 - CV4P0, (G - 64 - NCMB) * 6);
.LBB0_464:
	v_writelane_b32 v247, s22, 0
	v_writelane_b32 v247, s23, 1
	v_writelane_b32 v247, s24, 2
	v_writelane_b32 v247, s25, 3
	v_writelane_b32 v247, s26, 4
	v_writelane_b32 v247, s27, 5
	v_writelane_b32 v247, s28, 6
	v_writelane_b32 v247, s29, 7
	v_writelane_b32 v247, s30, 8
	v_writelane_b32 v247, s31, 9
	v_writelane_b32 v247, s32, 10
	v_writelane_b32 v247, s33, 11
	s_mov_b64 exec, -1
	s_waitcnt vmcnt(0)
	v_readlane_b32 s3, v246, 21
	s_nop 3
	s_cmpk_gt_i32 s94, 0xbf
	s_cbranch_scc1 .Lfc4_conv
	s_sub_i32 s2, s94, 64
	s_lshl_b32 s2, s2, 3
	s_add_i32 s2, s2, s3
	s_add_i32 s2, s2, 11264
	s_mov_b32 s4, 14336
	s_movk_i32 s33, 1024
	s_branch .Lfc4_go
.Lfc4_conv:
	s_sub_i32 s2, s94, 192
	s_lshl_b32 s2, s2, 3
	s_add_i32 s2, s2, s3
	s_mov_b32 s4, 11264
	s_movk_i32 s33, 512
